# T4+A4: gemm2 stage head reuses the MoE block tables gemm1 left in LDS (rebuild skipped); attention pass set-up no longer drains the two branch-gate loads before the first K/V DMA (consumed after branc
# speedup vs baseline: 1.0182x; 1.0066x over previous
.LBB0_830:
	s_or_b64 exec, exec, s[0:1]
	s_lshl_b64 s[0:1], 2, s66
	s_add_u32 s0, s0, -1
	s_addc_u32 s1, s1, -1
	s_cmp_lg_u32 s66, 63
	s_cselect_b32 s9, s1, -1
	s_cselect_b32 s8, s0, -1
	s_add_i32 s0, 0, 0x20000
	v_mov_b32_e32 v3, s0
	s_waitcnt lgkmcnt(0)
	s_barrier
	ds_read_b128 v[4:7], v3
	s_lshl_b64 s[6:7], 1, s66
	v_writelane_b32 v255, s8, 23
	s_mov_b32 m0, s69
	v_mov_b32_e32 v177, v169
	s_waitcnt lgkmcnt(0)
	v_readfirstlane_b32 s1, v5
	v_readfirstlane_b32 s0, v4
	v_readfirstlane_b32 s3, v7
	v_readfirstlane_b32 s2, v6
	s_or_b64 s[0:1], s[6:7], s[0:1]
	v_writelane_b32 v255, s9, 24
	s_or_b64 s[0:1], s[0:1], s[2:3]
	v_readlane_b32 s2, v255, 1
	v_readlane_b32 s3, v255, 2
	s_movk_i32 s6, 0xe000
	s_or_b32 s0, s0, 1
	v_lshl_add_u64 v[172:173], v[0:1], 0, s[2:3]
	v_readlane_b32 s2, v255, 7
	v_lshlrev_b64 v[184:185], 10, v[172:173]
	v_readlane_b32 s3, v255, 8
	s_and_b64 s[0:1], s[0:1], s[8:9]
	v_mov_b32_e32 v179, v169
	v_lshl_add_u64 v[0:1], s[2:3], 0, v[184:185]
	s_mov_b32 s2, 0x1000000
	v_add_co_u32_e32 v4, vcc, s2, v0
	v_readlane_b32 s2, v254, 50
	s_nop 0
	v_addc_co_u32_e32 v5, vcc, 0, v1, vcc
	global_load_dwordx3 v[160:162], v[0:1], off
	global_load_dwordx3 v[164:166], v[4:5], off
	v_add_u32_e32 v0, s2, v2
	v_ashrrev_i32_e32 v3, 4, v0
	v_xor_b32_e32 v4, v3, v2
	v_lshlrev_b32_e32 v1, 4, v2
	v_mul_lo_u32 v3, v3, s67
	v_lshlrev_b32_e32 v4, 4, v4
	s_movk_i32 s2, 0xf0
	s_movk_i32 s3, 0x70
	v_and_or_b32 v168, v4, s2, v3
	v_lshlrev_b32_e32 v3, 10, v0
	v_bitop3_b32 v4, v1, s3, v2 bitop3:0x48
	v_add_u32_e32 v0, 64, v0
	v_and_or_b32 v176, v3, s6, v4
	v_ashrrev_i32_e32 v3, 4, v0
	v_xor_b32_e32 v2, v3, v2
	v_mul_lo_u32 v3, v3, s67
	v_lshlrev_b32_e32 v2, 4, v2
	v_and_or_b32 v178, v2, s2, v3
	v_lshlrev_b32_e32 v2, 10, v0
	v_bitop3_b32 v0, v0, s3, v1 bitop3:0x48
	s_add_u32 s2, s0, -1
	v_and_or_b32 v180, v2, s6, v0
	s_addc_u32 s3, s1, -1
	s_add_i32 s6, s69, 0x4000
	global_load_lds_dwordx4 v168, s[92:93]
	v_writelane_b32 v255, s6, 25
	s_mov_b32 m0, s6
	s_add_i32 s6, s69, 0x400
	global_load_lds_dwordx4 v176, s[82:83]
	v_writelane_b32 v255, s6, 26
	s_mov_b32 m0, s6
	s_add_i32 s6, s69, 0x4400
	global_load_lds_dwordx4 v178, s[92:93]
	s_mov_b32 m0, s6
	s_and_b64 s[0:1], s[2:3], s[0:1]
	global_load_lds_dwordx4 v180, s[82:83]
	s_cmp_eq_u64 s[0:1], 0
	v_writelane_b32 v255, s6, 27
	s_cselect_b64 s[6:7], -1, 0
	s_ff1_i32_b64 s84, s[0:1]
	v_mov_b32_e32 v181, v169
	s_and_b64 vcc, exec, s[6:7]
	s_cbranch_vccnz .LBB0_832
	s_mul_i32 s2, s84, 0xc8000
	s_add_u32 s2, s92, s2
	s_addc_u32 s3, s93, 0
	s_lshl_b64 s[8:9], s[84:85], 7
	s_add_u32 s8, s82, s8
	s_addc_u32 s9, s83, s9
	v_lshl_add_u64 v[0:1], s[2:3], 0, v[168:169]
	s_add_i32 m0, s69, 0x8000
	s_nop 0
	global_load_lds_dwordx4 v[0:1], off
	v_lshl_add_u64 v[0:1], s[8:9], 0, v[176:177]
	s_add_i32 m0, s69, 0xc000
	s_nop 0
	global_load_lds_dwordx4 v[0:1], off
	v_lshl_add_u64 v[0:1], s[2:3], 0, v[178:179]
	v_readlane_b32 s2, v254, 57
	s_mov_b32 m0, s2
	v_readlane_b32 s2, v254, 58
	global_load_lds_dwordx4 v[0:1], off
	v_lshl_add_u64 v[0:1], s[8:9], 0, v[180:181]
	s_mov_b32 m0, s2
	s_nop 0
	global_load_lds_dwordx4 v[0:1], off

.LBB0_1483:
	s_or_b64 exec, exec, s[0:1]
	s_mov_b64 s[0:1], 0
	s_waitcnt lgkmcnt(0)
	v_mov_b32_e32 v0, v169
	s_barrier
	s_add_u32 s8, s76, s0
	v_mbcnt_lo_u32_b32 v0, -1, v0
	v_mbcnt_hi_u32_b32 v0, -1, v0
	v_or_b32_e32 v0, s75, v0
	s_addc_u32 s9, s77, s1
	s_mov_b32 s36, s74
	v_cmp_gt_i32_e32 vcc, 64, v0
	v_ashrrev_i32_e32 v1, 31, v0
	s_barrier
	s_and_saveexec_b64 s[0:1], vcc
	s_branch .LBB0_1486
	s_lshl_b32 s2, s82, 6
	s_ashr_i32 s3, s2, 31
	s_lshl_b64 s[2:3], s[2:3], 2
	s_add_u32 s2, s8, s2
	s_addc_u32 s3, s9, s3
	v_lshl_add_u64 v[2:3], v[0:1], 2, s[2:3]
	v_add_co_u32_e32 v2, vcc, 0x8000, v2
	v_lshl_add_u32 v4, v0, 2, 0
	s_nop 0
	v_addc_co_u32_e32 v3, vcc, 0, v3, vcc
	global_load_dword v2, v[2:3], off
	v_add_u32_e32 v5, 0x25c80, v4
	v_add_u32_e32 v6, -2, v199
	v_add_u32_e32 v4, 0x25000, v4
	s_waitcnt vmcnt(0)
	v_add_u32_e32 v3, 0xff, v2
	ds_write_b32 v5, v2
	v_and_b32_e32 v2, 64, v199
	v_add_u32_e32 v5, -1, v199
	v_cmp_lt_i32_e32 vcc, v5, v2
	v_and_b32_e32 v3, 0xffffff00, v3
	s_nop 0
	v_cndmask_b32_e32 v5, v5, v199, vcc
	v_lshlrev_b32_e32 v5, 2, v5
	ds_bpermute_b32 v5, v5, v3
	v_cmp_lt_i32_e32 vcc, 0, v0
	s_waitcnt lgkmcnt(0)
	s_nop 0
	v_cndmask_b32_e32 v5, 0, v5, vcc
	v_cmp_lt_i32_e32 vcc, v6, v2
	v_add_u32_e32 v5, v5, v3
	s_nop 0
	v_cndmask_b32_e32 v6, v6, v199, vcc
	v_lshlrev_b32_e32 v6, 2, v6
	ds_bpermute_b32 v6, v6, v5
	v_cmp_lt_i32_e32 vcc, 1, v0
	s_waitcnt lgkmcnt(0)
	s_nop 0
	v_cndmask_b32_e32 v6, 0, v6, vcc
	v_add_u32_e32 v5, v6, v5
	v_add_u32_e32 v6, -4, v199
	v_cmp_lt_i32_e32 vcc, v6, v2
	s_nop 1
	v_cndmask_b32_e32 v6, v6, v199, vcc
	v_lshlrev_b32_e32 v6, 2, v6
	ds_bpermute_b32 v6, v6, v5
	v_cmp_lt_i32_e32 vcc, 3, v0
	s_waitcnt lgkmcnt(0)
	s_nop 0
	v_cndmask_b32_e32 v6, 0, v6, vcc
	v_add_u32_e32 v5, v6, v5
	v_add_u32_e32 v6, -8, v199
	v_cmp_lt_i32_e32 vcc, v6, v2
	s_nop 1
	v_cndmask_b32_e32 v6, v6, v199, vcc
	v_lshlrev_b32_e32 v6, 2, v6
	ds_bpermute_b32 v6, v6, v5
	v_cmp_lt_i32_e32 vcc, 7, v0
	s_waitcnt lgkmcnt(0)
	s_nop 0
	v_cndmask_b32_e32 v6, 0, v6, vcc
	v_add_u32_e32 v5, v6, v5
	v_add_u32_e32 v6, -16, v199
	v_cmp_lt_i32_e32 vcc, v6, v2
	s_nop 1
	v_cndmask_b32_e32 v6, v6, v199, vcc
	v_lshlrev_b32_e32 v6, 2, v6
	ds_bpermute_b32 v6, v6, v5
	v_cmp_lt_i32_e32 vcc, 15, v0
	s_waitcnt lgkmcnt(0)
	s_nop 0
	v_cndmask_b32_e32 v6, 0, v6, vcc
	v_add_u32_e32 v5, v6, v5
	v_subrev_u32_e32 v6, 32, v199
	v_cmp_lt_i32_e32 vcc, v6, v2
	s_nop 1
	v_cndmask_b32_e32 v2, v6, v199, vcc
	v_lshlrev_b32_e32 v2, 2, v2
	ds_bpermute_b32 v2, v2, v5
	v_cmp_lt_i32_e32 vcc, 31, v0
	s_waitcnt lgkmcnt(0)
	s_nop 0
	v_cndmask_b32_e32 v2, 0, v2, vcc
	v_add_u32_e32 v2, v2, v5
	v_sub_u32_e32 v3, v2, v3
	v_cmp_eq_u32_e32 vcc, 63, v0
	ds_write_b32 v4, v3
	s_and_b64 exec, exec, vcc
	s_cbranch_execz .LBB0_1486
	v_readlane_b32 s2, v254, 11
	s_nop 1
	v_mov_b32_e32 v3, s2
	ds_write_b32 v3, v2
.LBB0_1486:
	s_or_b64 exec, exec, s[0:1]
	s_movk_i32 s0, 0x240
	v_cmp_gt_i32_e32 vcc, s0, v0
	s_waitcnt lgkmcnt(0)
	s_barrier
	s_and_saveexec_b64 s[2:3], vcc
	s_branch .LBB0_1489
	v_readlane_b32 s0, v254, 12
	v_add_u32_e32 v2, 0xfffffe00, v0
	v_lshlrev_b32_e32 v4, 8, v0
	v_lshl_add_u32 v3, v0, 2, s0
	s_mov_b64 s[4:5], 0
